# speedup vs baseline: 1.0018x; 1.0018x over previous
.Llight_path:
	s_lshr_b32 s27, s7, 8
	s_waitcnt vmcnt(16)
	s_add_u32 s30, s8, 0x3000
	s_addc_u32 s31, s9, 0
	s_add_u32 s28, s27, 1
	s_and_b32 s28, s28, 7
	s_lshl_b32 s28, s28, 10
	v_add_u32_e32 v246, s28, v210
	s_add_u32 s28, s27, 2
	s_and_b32 s28, s28, 7
	s_lshl_b32 s28, s28, 10
	v_add_u32_e32 v247, s28, v210
	s_add_u32 s28, s27, 3
	s_and_b32 s28, s28, 7
	s_lshl_b32 s28, s28, 10
	v_add_u32_e32 v248, s28, v210
	s_add_u32 s28, s27, 4
	s_and_b32 s28, s28, 7
	s_lshl_b32 s28, s28, 10
	v_add_u32_e32 v249, s28, v210
	s_add_u32 s28, s27, 5
	s_and_b32 s28, s28, 7
	s_lshl_b32 s28, s28, 10
	v_add_u32_e32 v250, s28, v210
	s_add_u32 s28, s27, 6
	s_and_b32 s28, s28, 7
	s_lshl_b32 s28, s28, 10
	v_add_u32_e32 v251, s28, v210
	s_add_u32 s28, s27, 7
	s_and_b32 s28, s28, 7
	s_lshl_b32 s28, s28, 10
	v_add_u32_e32 v252, s28, v210
	s_add_u32 s28, s27, 8
	s_and_b32 s28, s28, 7
	s_lshl_b32 s28, s28, 10
	v_add_u32_e32 v253, s28, v210
	global_load_dwordx4 v[126:129], v246, s[8:9]
	global_load_dwordx4 v[78:81], v246, s[30:31]
	global_load_dwordx4 v[122:125], v247, s[8:9]
	global_load_dwordx4 v[74:77], v247, s[30:31]
	global_load_dwordx4 v[118:121], v248, s[8:9]
	global_load_dwordx4 v[70:73], v248, s[30:31]
	global_load_dwordx4 v[114:117], v249, s[8:9]
	global_load_dwordx4 v[66:69], v249, s[30:31]
	global_load_dwordx4 v[110:113], v250, s[8:9]
	global_load_dwordx4 v[62:65], v250, s[30:31]
	global_load_dwordx4 v[106:109], v251, s[8:9]
	global_load_dwordx4 v[58:61], v251, s[30:31]
	global_load_dwordx4 v[102:105], v252, s[8:9]
	global_load_dwordx4 v[54:57], v252, s[30:31]
	global_load_dwordx4 v[98:101], v253, s[8:9]
	global_load_dwordx4 v[50:53], v253, s[30:31]
	v_mul_u32_u24_e32 v236, 36, v228
	v_add_u32_e32 v236, v236, v230
	v_add_u32_e32 v237, s7, v229
	v_mul_u32_u24_e32 v238, 0x104, v228
	v_add_u32_e32 v238, v238, v237
	v_add_u32_e32 v238, 0xb840, v238
	v_add_u32_e32 v231, s7, v229
	v_add_u32_e32 v231, 0xb840, v231
	v_add_u32_e32 v211, s6, v210
	s_nop 0
	s_load_dwordx8 s[4:11], s[0:1], 0x10
	v_add_u32_e32 v232, 0x24e80, v228
	ds_read_b32 v244, v232
	ds_read_b32 v245, v232 offset:128
	ds_read_b128 v[194:197], v237 offset:36928
	ds_read_b128 v[198:201], v237 offset:36944
	ds_read_b128 v[202:205], v237 offset:36960
	ds_read_b128 v[206:209], v237 offset:36976
	ds_read_b128 v[212:215], v237 offset:37056
	ds_read_b128 v[216:219], v237 offset:37072
	ds_read_b128 v[220:223], v237 offset:37088
	ds_read_b128 v[224:227], v237 offset:37104
	ds_read_b128 v[162:165], v236 offset:16384
	ds_read_b128 v[166:169], v236 offset:16416
	ds_read_b128 v[170:173], v236 offset:16448
	ds_read_b128 v[174:177], v236 offset:16480
	s_waitcnt lgkmcnt(0)
	v_mfma_f32_32x32x16_bf16 v[2:17], v[94:97], v[162:165], v[194:209]
	v_mfma_f32_32x32x16_bf16 v[18:33], v[46:49], v[162:165], v[212:227]
	v_mfma_f32_32x32x16_bf16 v[2:17], v[90:93], v[166:169], v[2:17]
	v_mfma_f32_32x32x16_bf16 v[18:33], v[42:45], v[166:169], v[18:33]
	v_mfma_f32_32x32x16_bf16 v[2:17], v[86:89], v[170:173], v[2:17]
	ds_read_b128 v[178:181], v236 offset:20992
	v_mfma_f32_32x32x16_bf16 v[18:33], v[38:41], v[170:173], v[18:33]
	ds_read_b128 v[182:185], v236 offset:21024
	v_mfma_f32_32x32x16_bf16 v[2:17], v[82:85], v[174:177], v[2:17]
	ds_read_b128 v[186:189], v236 offset:21056
	v_mfma_f32_32x32x16_bf16 v[18:33], v[34:37], v[174:177], v[18:33]
	ds_read_b128 v[190:193], v236 offset:21088
	s_waitcnt lgkmcnt(0)
	v_mfma_f32_32x32x16_bf16 v[130:145], v[94:97], v[178:181], v[194:209]
	v_mfma_f32_32x32x16_bf16 v[146:161], v[46:49], v[178:181], v[212:227]
	v_mfma_f32_32x32x16_bf16 v[130:145], v[90:93], v[182:185], v[130:145]
	v_mfma_f32_32x32x16_bf16 v[146:161], v[42:45], v[182:185], v[146:161]
	s_nop 7
	ds_write_b128 v238, v[2:5] offset:0
	ds_write_b128 v238, v[6:9] offset:16
	ds_write_b128 v238, v[10:13] offset:32
	ds_write_b128 v238, v[14:17] offset:48
	ds_write_b128 v238, v[18:21] offset:128
	ds_write_b128 v238, v[22:25] offset:144
	ds_write_b128 v238, v[26:29] offset:160
	ds_write_b128 v238, v[30:33] offset:176
	v_mfma_f32_32x32x16_bf16 v[130:145], v[86:89], v[186:189], v[130:145]
	ds_read_b128 v[162:165], v236 offset:25600
	v_mfma_f32_32x32x16_bf16 v[146:161], v[38:41], v[186:189], v[146:161]
	ds_read_b128 v[166:169], v236 offset:25632
	v_mfma_f32_32x32x16_bf16 v[130:145], v[82:85], v[190:193], v[130:145]
	ds_read_b128 v[170:173], v236 offset:25664
	v_mfma_f32_32x32x16_bf16 v[146:161], v[34:37], v[190:193], v[146:161]
	ds_read_b128 v[174:177], v236 offset:25696
	s_waitcnt lgkmcnt(0)
	v_mfma_f32_32x32x16_bf16 v[2:17], v[94:97], v[162:165], v[194:209]
	v_mfma_f32_32x32x16_bf16 v[18:33], v[46:49], v[162:165], v[212:227]
	v_mfma_f32_32x32x16_bf16 v[2:17], v[90:93], v[166:169], v[2:17]
	v_mfma_f32_32x32x16_bf16 v[18:33], v[42:45], v[166:169], v[18:33]
	s_nop 7
	v_add_u32_e32 v239, 0x8200, v238
	ds_write_b128 v239, v[130:133] offset:0
	ds_write_b128 v239, v[134:137] offset:16
	ds_write_b128 v239, v[138:141] offset:32
	ds_write_b128 v239, v[142:145] offset:48
	ds_write_b128 v239, v[146:149] offset:128
	ds_write_b128 v239, v[150:153] offset:144
	ds_write_b128 v239, v[154:157] offset:160
	ds_write_b128 v239, v[158:161] offset:176
	v_mfma_f32_32x32x16_bf16 v[2:17], v[86:89], v[170:173], v[2:17]
	ds_read_b128 v[178:181], v236 offset:30208
	v_mfma_f32_32x32x16_bf16 v[18:33], v[38:41], v[170:173], v[18:33]
	ds_read_b128 v[182:185], v236 offset:30240
	v_mfma_f32_32x32x16_bf16 v[2:17], v[82:85], v[174:177], v[2:17]
	ds_read_b128 v[186:189], v236 offset:30272
	v_mfma_f32_32x32x16_bf16 v[18:33], v[34:37], v[174:177], v[18:33]
	ds_read_b128 v[190:193], v236 offset:30304
	s_waitcnt lgkmcnt(0)
	v_mfma_f32_32x32x16_bf16 v[130:145], v[94:97], v[178:181], v[194:209]
	v_mfma_f32_32x32x16_bf16 v[146:161], v[46:49], v[178:181], v[212:227]
	v_mfma_f32_32x32x16_bf16 v[130:145], v[90:93], v[182:185], v[130:145]
	v_mfma_f32_32x32x16_bf16 v[146:161], v[42:45], v[182:185], v[146:161]
	s_nop 7
	v_add_u32_e32 v239, 0x10400, v238
	ds_write_b128 v239, v[2:5] offset:0
	ds_write_b128 v239, v[6:9] offset:16
	ds_write_b128 v239, v[10:13] offset:32
	ds_write_b128 v239, v[14:17] offset:48
	ds_write_b128 v239, v[18:21] offset:128
	ds_write_b128 v239, v[22:25] offset:144
	ds_write_b128 v239, v[26:29] offset:160
	ds_write_b128 v239, v[30:33] offset:176
	v_mfma_f32_32x32x16_bf16 v[130:145], v[86:89], v[186:189], v[130:145]
	v_mfma_f32_32x32x16_bf16 v[146:161], v[38:41], v[186:189], v[146:161]
	v_mfma_f32_32x32x16_bf16 v[130:145], v[82:85], v[190:193], v[130:145]
	v_mfma_f32_32x32x16_bf16 v[146:161], v[34:37], v[190:193], v[146:161]
	s_nop 7
	s_nop 7
	v_cmp_gt_u32_e32 vcc, 16, v228
	s_and_saveexec_b64 s[20:21], vcc
	v_add_u32_e32 v239, 0x18600, v238
	ds_write_b128 v239, v[130:133] offset:0
	ds_write_b128 v239, v[134:137] offset:16
	ds_write_b128 v239, v[138:141] offset:32
	ds_write_b128 v239, v[142:145] offset:48
	ds_write_b128 v239, v[146:149] offset:128
	ds_write_b128 v239, v[150:153] offset:144
	ds_write_b128 v239, v[154:157] offset:160
	ds_write_b128 v239, v[158:161] offset:176
	s_or_b64 exec, exec, s[20:21]
	s_mov_b32 s12, 0xbeb17218
	v_mov_b32_e32 v235, 0xc038aa3b
	v_add_u32_e32 v233, v231, v244
	v_add_u32_e32 v234, v231, v245
	ds_read_b128 v[2:5], v233 offset:0
	ds_read_b128 v[6:9], v233 offset:16
	ds_read_b128 v[10:13], v233 offset:32
	ds_read_b128 v[14:17], v233 offset:48
	ds_read_b128 v[18:21], v233 offset:128
	ds_read_b128 v[22:25], v233 offset:144
	ds_read_b128 v[26:29], v233 offset:160
	ds_read_b128 v[30:33], v233 offset:176
	ds_read_b128 v[34:37], v234 offset:0
	ds_read_b128 v[38:41], v234 offset:16
	ds_read_b128 v[42:45], v234 offset:32
	ds_read_b128 v[46:49], v234 offset:48
	v_mov_b32_e32 v194, 0
	v_mov_b32_e32 v195, 0
	v_mov_b32_e32 v196, 0
	v_mov_b32_e32 v197, 0
	v_mov_b32_e32 v198, 0
	v_mov_b32_e32 v199, 0
	v_mov_b32_e32 v200, 0
	v_mov_b32_e32 v201, 0
	v_mov_b32_e32 v202, 0
	v_mov_b32_e32 v203, 0
	v_mov_b32_e32 v204, 0
	v_mov_b32_e32 v205, 0
	v_mov_b32_e32 v206, 0
	v_mov_b32_e32 v207, 0
	v_mov_b32_e32 v208, 0
	v_mov_b32_e32 v209, 0
	v_add_u32_e32 v232, 0x100, v232
	s_movk_i32 s16, 18
	s_add_u32 s28, s27, 1
	s_and_b32 s28, s28, 7
	s_lshl_b32 s28, s28, 10
	v_add_u32_e32 v158, s28, v210
	s_add_u32 s28, s27, 2
	s_and_b32 s28, s28, 7
	s_lshl_b32 s28, s28, 10
	v_add_u32_e32 v159, s28, v210
	s_add_u32 s28, s27, 3
	s_and_b32 s28, s28, 7
	s_lshl_b32 s28, s28, 10
	v_add_u32_e32 v160, s28, v210
	s_add_u32 s28, s27, 4
	s_and_b32 s28, s28, 7
	s_lshl_b32 s28, s28, 10
	v_add_u32_e32 v161, s28, v210
	s_add_u32 s28, s27, 5
	s_and_b32 s28, s28, 7
	s_lshl_b32 s28, s28, 10
	v_add_u32_e32 v190, s28, v210
	s_add_u32 s28, s27, 6
	s_and_b32 s28, s28, 7
	s_lshl_b32 s28, s28, 10
	v_add_u32_e32 v191, s28, v210
	s_add_u32 s28, s27, 7
	s_and_b32 s28, s28, 7
	s_lshl_b32 s28, s28, 10
	v_add_u32_e32 v192, s28, v210
	s_waitcnt vmcnt(0) lgkmcnt(0)
	ds_read_b128 v[82:85], v234 offset:128
	ds_read_b128 v[86:89], v234 offset:144
	ds_read_b128 v[90:93], v234 offset:160
	ds_read_b128 v[94:97], v234 offset:176
	ds_read2_b32 v[244:245], v232 offset1:32
	v_exp_f32_e32 v212, v4
	v_exp_f32_e32 v213, v8
	v_exp_f32_e32 v214, v12
	v_exp_f32_e32 v215, v16
	v_exp_f32_e32 v216, v2
	v_fma_f32 v251, v212, s12, s12
	v_exp_f32_e32 v217, v6
	v_fma_f32 v252, v213, s12, s12
	v_exp_f32_e32 v218, v10
	v_fma_f32 v253, v214, s12, s12
	v_exp_f32_e32 v219, v14
	v_fma_f32 v254, v215, s12, s12
	v_fmac_f32_e32 v251, v216, v251
	v_fmac_f32_e32 v252, v217, v252
	v_fmac_f32_e32 v253, v218, v253
	v_fmac_f32_e32 v254, v219, v254
	v_rcp_f32_e32 v216, v251
	v_rcp_f32_e32 v217, v252
	v_rcp_f32_e32 v218, v253
	v_rcp_f32_e32 v219, v254
	v_exp_f32_e32 v246, v5
	v_fma_f32 v194, -v212, v216, v216
	v_exp_f32_e32 v247, v9
	v_fma_f32 v195, -v213, v217, v217
	v_exp_f32_e32 v248, v13
	v_fma_f32 v196, -v214, v218, v218
	v_exp_f32_e32 v249, v17
	v_fma_f32 v197, -v215, v219, v219
	v_exp_f32_e32 v212, v194
	v_add_f32_e32 v246, 1.0, v246
	v_exp_f32_e32 v213, v195
	v_add_f32_e32 v247, 1.0, v247
	v_exp_f32_e32 v214, v196
	v_add_f32_e32 v248, 1.0, v248
	v_exp_f32_e32 v215, v197
	v_add_f32_e32 v249, 1.0, v249
	v_fmac_f32_e32 v246, v246, v212
	v_fmac_f32_e32 v247, v247, v213
	v_fmac_f32_e32 v248, v248, v214
	v_fmac_f32_e32 v249, v249, v215
	v_rcp_f32_e32 v246, v246
	v_rcp_f32_e32 v247, v247
	v_rcp_f32_e32 v248, v248
	v_rcp_f32_e32 v249, v249
	v_fma_f32 v246, -v212, v246, v246
	v_fma_f32 v247, -v213, v247, v247
	v_fma_f32 v248, -v214, v248, v248
	v_fma_f32 v249, -v215, v249, v249
	v_cvt_pk_bf16_f32 v236, v246, v247
	v_cvt_pk_bf16_f32 v237, v248, v249
	s_waitcnt lgkmcnt(0)
	v_add_u32_e32 v233, v231, v244
	ds_read_b128 v[2:5], v233 offset:0
	ds_read_b128 v[6:9], v233 offset:16
	ds_read_b128 v[10:13], v233 offset:32
	ds_read_b128 v[14:17], v233 offset:48
	v_exp_f32_e32 v212, v20
	v_exp_f32_e32 v213, v24
	v_exp_f32_e32 v214, v28
	v_exp_f32_e32 v215, v32
	v_exp_f32_e32 v216, v18
	v_fma_f32 v251, v212, s12, s12
	v_exp_f32_e32 v217, v22
	v_fma_f32 v252, v213, s12, s12
	v_exp_f32_e32 v218, v26
	v_fma_f32 v253, v214, s12, s12
	v_exp_f32_e32 v219, v30
	v_fma_f32 v254, v215, s12, s12
	v_fmac_f32_e32 v251, v216, v251
	v_fmac_f32_e32 v252, v217, v252
	v_fmac_f32_e32 v253, v218, v253
	v_fmac_f32_e32 v254, v219, v254
	v_rcp_f32_e32 v216, v251
	v_rcp_f32_e32 v217, v252
	v_rcp_f32_e32 v218, v253
	v_rcp_f32_e32 v219, v254
	v_exp_f32_e32 v246, v21
	v_fma_f32 v198, -v212, v216, v216
	v_exp_f32_e32 v247, v25
	v_fma_f32 v199, -v213, v217, v217
	v_exp_f32_e32 v248, v29
	v_fma_f32 v200, -v214, v218, v218
	v_exp_f32_e32 v249, v33
	v_fma_f32 v201, -v215, v219, v219
	v_exp_f32_e32 v212, v198
	v_add_f32_e32 v246, 1.0, v246
	v_exp_f32_e32 v213, v199
	v_add_f32_e32 v247, 1.0, v247
	v_exp_f32_e32 v214, v200
	v_add_f32_e32 v248, 1.0, v248
	v_exp_f32_e32 v215, v201
	v_add_f32_e32 v249, 1.0, v249
	v_fmac_f32_e32 v246, v246, v212
	v_fmac_f32_e32 v247, v247, v213
	v_fmac_f32_e32 v248, v248, v214
	v_fmac_f32_e32 v249, v249, v215
	v_rcp_f32_e32 v246, v246
	v_rcp_f32_e32 v247, v247
	v_rcp_f32_e32 v248, v248
	v_rcp_f32_e32 v249, v249
	v_fma_f32 v246, -v212, v246, v246
	v_fma_f32 v247, -v213, v247, v247
	v_fma_f32 v248, -v214, v248, v248
	v_fma_f32 v249, -v215, v249, v249
	v_cvt_pk_bf16_f32 v238, v246, v247
	v_cvt_pk_bf16_f32 v239, v248, v249
	ds_write_b128 v211, v[236:239] offset:0
	ds_read_b128 v[18:21], v233 offset:128
	ds_read_b128 v[22:25], v233 offset:144
	ds_read_b128 v[26:29], v233 offset:160
	ds_read_b128 v[30:33], v233 offset:176
	v_exp_f32_e32 v212, v36
	v_exp_f32_e32 v213, v40
	v_exp_f32_e32 v214, v44
	v_exp_f32_e32 v215, v48
	s_waitcnt lgkmcnt(4)
	s_barrier
	ds_read_b128 v[130:133], v158 offset:0
	ds_read_b128 v[134:137], v159 offset:0
	v_exp_f32_e32 v216, v34
	v_fma_f32 v251, v212, s12, s12
	v_exp_f32_e32 v217, v38
	v_fma_f32 v252, v213, s12, s12
	v_exp_f32_e32 v218, v42
	v_fma_f32 v253, v214, s12, s12
	v_exp_f32_e32 v219, v46
	v_fma_f32 v254, v215, s12, s12
	ds_read_b128 v[138:141], v160 offset:0
	ds_read_b128 v[142:145], v161 offset:0
	v_fmac_f32_e32 v251, v216, v251
	v_fmac_f32_e32 v252, v217, v252
	v_fmac_f32_e32 v253, v218, v253
	v_fmac_f32_e32 v254, v219, v254
	ds_read_b128 v[146:149], v190 offset:0
	ds_read_b128 v[150:153], v191 offset:0
	v_rcp_f32_e32 v216, v251
	v_rcp_f32_e32 v217, v252
	v_rcp_f32_e32 v218, v253
	v_rcp_f32_e32 v219, v254
	ds_read_b128 v[154:157], v192 offset:0
	v_exp_f32_e32 v246, v37
	v_fma_f32 v202, -v212, v216, v216
	v_exp_f32_e32 v247, v41
	v_fma_f32 v203, -v213, v217, v217
	v_exp_f32_e32 v248, v45
	v_fma_f32 v204, -v214, v218, v218
	v_exp_f32_e32 v249, v49
	v_fma_f32 v205, -v215, v219, v219
	v_exp_f32_e32 v212, v202
	v_add_f32_e32 v246, 1.0, v246
	v_exp_f32_e32 v213, v203
	v_add_f32_e32 v247, 1.0, v247
	v_exp_f32_e32 v214, v204
	v_add_f32_e32 v248, 1.0, v248
	v_exp_f32_e32 v215, v205
	v_add_f32_e32 v249, 1.0, v249
	v_fmac_f32_e32 v246, v246, v212
	v_fmac_f32_e32 v247, v247, v213
	v_fmac_f32_e32 v248, v248, v214
	v_fmac_f32_e32 v249, v249, v215
	v_rcp_f32_e32 v246, v246
	v_rcp_f32_e32 v247, v247
	v_rcp_f32_e32 v248, v248
	v_rcp_f32_e32 v249, v249
	v_fma_f32 v246, -v212, v246, v246
	v_fma_f32 v247, -v213, v247, v247
	v_fma_f32 v248, -v214, v248, v248
	v_fma_f32 v249, -v215, v249, v249
	v_cvt_pk_bf16_f32 v224, v246, v247
	v_cvt_pk_bf16_f32 v225, v248, v249
	s_waitcnt lgkmcnt(0)
	v_mfma_f32_32x32x16_bf16 v[2:17], v[126:129], v[130:133], v[2:17]
	v_add_u32_e32 v234, v231, v245
	ds_read_b128 v[34:37], v234 offset:0
	ds_read_b128 v[38:41], v234 offset:16
	ds_read_b128 v[42:45], v234 offset:32
	ds_read_b128 v[46:49], v234 offset:48
	v_add_u32_e32 v232, 0x100, v232
	v_exp_f32_e32 v212, v84
	v_exp_f32_e32 v213, v88
	v_exp_f32_e32 v214, v92
	v_exp_f32_e32 v215, v96
	v_mfma_f32_32x32x16_bf16 v[2:17], v[122:125], v[134:137], v[2:17]
	v_exp_f32_e32 v216, v82
	v_fma_f32 v251, v212, s12, s12
	v_exp_f32_e32 v217, v86
	v_fma_f32 v252, v213, s12, s12
	v_exp_f32_e32 v218, v90
	v_fma_f32 v253, v214, s12, s12
	v_exp_f32_e32 v219, v94
	v_fma_f32 v254, v215, s12, s12
	v_mfma_f32_32x32x16_bf16 v[2:17], v[118:121], v[138:141], v[2:17]
	v_fmac_f32_e32 v251, v216, v251
	v_fmac_f32_e32 v252, v217, v252
	v_fmac_f32_e32 v253, v218, v253
	v_fmac_f32_e32 v254, v219, v254
	v_mfma_f32_32x32x16_bf16 v[2:17], v[114:117], v[142:145], v[2:17]
	v_rcp_f32_e32 v216, v251
	v_rcp_f32_e32 v217, v252
	v_rcp_f32_e32 v218, v253
	v_rcp_f32_e32 v219, v254
	v_mfma_f32_32x32x16_bf16 v[2:17], v[110:113], v[146:149], v[2:17]
	v_exp_f32_e32 v246, v85
	v_fma_f32 v206, -v212, v216, v216
	v_exp_f32_e32 v247, v89
	v_fma_f32 v207, -v213, v217, v217
	v_exp_f32_e32 v248, v93
	v_fma_f32 v208, -v214, v218, v218
	v_exp_f32_e32 v249, v97
	v_fma_f32 v209, -v215, v219, v219
	v_mfma_f32_32x32x16_bf16 v[2:17], v[106:109], v[150:153], v[2:17]
	v_mfma_f32_32x32x16_bf16 v[2:17], v[102:105], v[154:157], v[2:17]
	v_exp_f32_e32 v212, v206
	v_add_f32_e32 v246, 1.0, v246
	v_exp_f32_e32 v213, v207
	v_add_f32_e32 v247, 1.0, v247
	v_exp_f32_e32 v214, v208
	v_add_f32_e32 v248, 1.0, v248
	v_exp_f32_e32 v215, v209
	v_add_f32_e32 v249, 1.0, v249
	v_fmac_f32_e32 v246, v246, v212
	v_fmac_f32_e32 v247, v247, v213
	v_fmac_f32_e32 v248, v248, v214
	v_fmac_f32_e32 v249, v249, v215
	v_mfma_f32_32x32x16_bf16 v[2:17], v[98:101], v[236:239], v[2:17]
	v_rcp_f32_e32 v246, v246
	v_rcp_f32_e32 v247, v247
	v_rcp_f32_e32 v248, v248
	v_rcp_f32_e32 v249, v249
	v_fma_f32 v246, -v212, v246, v246
	v_fma_f32 v247, -v213, v247, v247
	v_fma_f32 v248, -v214, v248, v248
	v_fma_f32 v249, -v215, v249, v249
	v_cvt_pk_bf16_f32 v226, v246, v247
	v_cvt_pk_bf16_f32 v227, v248, v249
	ds_write_b128 v211, v[224:227] offset:8192
	.p2align 6
.Llight_loop:
	v_mfma_f32_32x32x16_bf16 v[18:33], v[78:81], v[130:133], v[18:33]
	ds_read_b128 v[82:85], v234 offset:128
	ds_read_b128 v[86:89], v234 offset:144
	ds_read_b128 v[90:93], v234 offset:160
	ds_read_b128 v[94:97], v234 offset:176
	ds_read2_b32 v[244:245], v232 offset1:32
	v_exp_f32_e32 v212, v4
	v_exp_f32_e32 v213, v8
	v_exp_f32_e32 v214, v12
	v_exp_f32_e32 v215, v16
	s_waitcnt lgkmcnt(5)
	s_barrier
	v_mfma_f32_32x32x16_bf16 v[18:33], v[74:77], v[134:137], v[18:33]
	ds_read_b128 v[162:165], v158 offset:8192
	ds_read_b128 v[166:169], v159 offset:8192
	v_exp_f32_e32 v216, v2
	v_fma_f32 v251, v212, s12, s12
	v_exp_f32_e32 v217, v6
	v_fma_f32 v252, v213, s12, s12
	v_exp_f32_e32 v218, v10
	v_fma_f32 v253, v214, s12, s12
	v_exp_f32_e32 v219, v14
	v_fma_f32 v254, v215, s12, s12
	v_mfma_f32_32x32x16_bf16 v[18:33], v[70:73], v[138:141], v[18:33]
	ds_read_b128 v[170:173], v160 offset:8192
	ds_read_b128 v[174:177], v161 offset:8192
	v_exp_f32_e32 v220, v3
	v_fmac_f32_e32 v251, v216, v251
	v_exp_f32_e32 v221, v7
	v_fmac_f32_e32 v252, v217, v252
	v_exp_f32_e32 v222, v11
	v_fmac_f32_e32 v253, v218, v253
	v_exp_f32_e32 v223, v15
	v_fmac_f32_e32 v254, v219, v254
	v_mfma_f32_32x32x16_bf16 v[18:33], v[66:69], v[142:145], v[18:33]
	ds_read_b128 v[178:181], v190 offset:8192
	ds_read_b128 v[182:185], v191 offset:8192
	v_rcp_f32_e32 v216, v251
	v_add_f32_e32 v220, 1.0, v220
	v_rcp_f32_e32 v217, v252
	v_add_f32_e32 v221, 1.0, v221
	v_rcp_f32_e32 v218, v253
	v_add_f32_e32 v222, 1.0, v222
	v_rcp_f32_e32 v219, v254
	v_add_f32_e32 v223, 1.0, v223
	v_mfma_f32_32x32x16_bf16 v[18:33], v[62:65], v[146:149], v[18:33]
	ds_read_b128 v[186:189], v192 offset:8192
	v_rcp_f32_e32 v220, v220
	v_fma_f32 v240, -v212, v216, v216
	v_rcp_f32_e32 v221, v221
	v_fma_f32 v241, -v213, v217, v217
	v_rcp_f32_e32 v222, v222
	v_fma_f32 v242, -v214, v218, v218
	v_rcp_f32_e32 v223, v223
	v_fma_f32 v243, -v215, v219, v219
	v_mfma_f32_32x32x16_bf16 v[18:33], v[58:61], v[150:153], v[18:33]
	v_exp_f32_e32 v246, v5
	v_fma_f32 v194, v220, v194, v240
	v_exp_f32_e32 v247, v9
	v_fma_f32 v195, v221, v195, v241
	v_exp_f32_e32 v248, v13
	v_fma_f32 v196, v222, v196, v242
	v_exp_f32_e32 v249, v17
	v_fma_f32 v197, v223, v197, v243
	v_mfma_f32_32x32x16_bf16 v[18:33], v[54:57], v[154:157], v[18:33]
	v_exp_f32_e32 v212, v194
	v_add_f32_e32 v246, 1.0, v246
	v_exp_f32_e32 v213, v195
	v_add_f32_e32 v247, 1.0, v247
	v_exp_f32_e32 v214, v196
	v_add_f32_e32 v248, 1.0, v248
	v_exp_f32_e32 v215, v197
	v_add_f32_e32 v249, 1.0, v249
	v_fmac_f32_e32 v246, v246, v212
	v_fmac_f32_e32 v247, v247, v213
	v_fmac_f32_e32 v248, v248, v214
	v_fmac_f32_e32 v249, v249, v215
	v_mfma_f32_32x32x16_bf16 v[18:33], v[50:53], v[236:239], v[18:33]
	v_rcp_f32_e32 v246, v246
	v_rcp_f32_e32 v247, v247
	v_rcp_f32_e32 v248, v248
	v_rcp_f32_e32 v249, v249
	v_fma_f32 v246, -v212, v246, v246
	v_fma_f32 v247, -v213, v247, v247
	v_fma_f32 v248, -v214, v248, v248
	v_fma_f32 v249, -v215, v249, v249
	v_cvt_pk_bf16_f32 v236, v246, v247
	v_cvt_pk_bf16_f32 v237, v248, v249
	s_waitcnt lgkmcnt(0)
	v_mfma_f32_32x32x16_bf16 v[34:49], v[126:129], v[162:165], v[34:49]
	v_add_u32_e32 v233, v231, v244
	ds_read_b128 v[2:5], v233 offset:0
	ds_read_b128 v[6:9], v233 offset:16
	ds_read_b128 v[10:13], v233 offset:32
	ds_read_b128 v[14:17], v233 offset:48
	v_exp_f32_e32 v212, v20
	v_exp_f32_e32 v213, v24
	v_exp_f32_e32 v214, v28
	v_exp_f32_e32 v215, v32
	v_mfma_f32_32x32x16_bf16 v[34:49], v[122:125], v[166:169], v[34:49]
	v_exp_f32_e32 v216, v18
	v_fma_f32 v251, v212, s12, s12
	v_exp_f32_e32 v217, v22
	v_fma_f32 v252, v213, s12, s12
	v_exp_f32_e32 v218, v26
	v_fma_f32 v253, v214, s12, s12
	v_exp_f32_e32 v219, v30
	v_fma_f32 v254, v215, s12, s12
	v_mfma_f32_32x32x16_bf16 v[34:49], v[118:121], v[170:173], v[34:49]
	v_exp_f32_e32 v220, v19
	v_fmac_f32_e32 v251, v216, v251
	v_exp_f32_e32 v221, v23
	v_fmac_f32_e32 v252, v217, v252
	v_exp_f32_e32 v222, v27
	v_fmac_f32_e32 v253, v218, v253
	v_exp_f32_e32 v223, v31
	v_fmac_f32_e32 v254, v219, v254
	v_mfma_f32_32x32x16_bf16 v[34:49], v[114:117], v[174:177], v[34:49]
	v_rcp_f32_e32 v216, v251
	v_add_f32_e32 v220, 1.0, v220
	v_rcp_f32_e32 v217, v252
	v_add_f32_e32 v221, 1.0, v221
	v_rcp_f32_e32 v218, v253
	v_add_f32_e32 v222, 1.0, v222
	v_rcp_f32_e32 v219, v254
	v_add_f32_e32 v223, 1.0, v223
	v_mfma_f32_32x32x16_bf16 v[34:49], v[110:113], v[178:181], v[34:49]
	v_rcp_f32_e32 v220, v220
	v_fma_f32 v240, -v212, v216, v216
	v_rcp_f32_e32 v221, v221
	v_fma_f32 v241, -v213, v217, v217
	v_rcp_f32_e32 v222, v222
	v_fma_f32 v242, -v214, v218, v218
	v_rcp_f32_e32 v223, v223
	v_fma_f32 v243, -v215, v219, v219
	v_mfma_f32_32x32x16_bf16 v[34:49], v[106:109], v[182:185], v[34:49]
	v_exp_f32_e32 v246, v21
	v_fma_f32 v198, v220, v198, v240
	v_exp_f32_e32 v247, v25
	v_fma_f32 v199, v221, v199, v241
	v_exp_f32_e32 v248, v29
	v_fma_f32 v200, v222, v200, v242
	v_exp_f32_e32 v249, v33
	v_fma_f32 v201, v223, v201, v243
	v_mfma_f32_32x32x16_bf16 v[34:49], v[102:105], v[186:189], v[34:49]
	v_exp_f32_e32 v212, v198
	v_add_f32_e32 v246, 1.0, v246
	v_exp_f32_e32 v213, v199
	v_add_f32_e32 v247, 1.0, v247
	v_exp_f32_e32 v214, v200
	v_add_f32_e32 v248, 1.0, v248
	v_exp_f32_e32 v215, v201
	v_add_f32_e32 v249, 1.0, v249
	v_fmac_f32_e32 v246, v246, v212
	v_fmac_f32_e32 v247, v247, v213
	v_fmac_f32_e32 v248, v248, v214
	v_fmac_f32_e32 v249, v249, v215
	v_mfma_f32_32x32x16_bf16 v[34:49], v[98:101], v[224:227], v[34:49]
	v_rcp_f32_e32 v246, v246
	v_rcp_f32_e32 v247, v247
	v_rcp_f32_e32 v248, v248
	v_rcp_f32_e32 v249, v249
	v_fma_f32 v246, -v212, v246, v246
	v_fma_f32 v247, -v213, v247, v247
	v_fma_f32 v248, -v214, v248, v248
	v_fma_f32 v249, -v215, v249, v249
	v_cvt_pk_bf16_f32 v238, v246, v247
	v_cvt_pk_bf16_f32 v239, v248, v249
	ds_write_b128 v211, v[236:239] offset:0
	v_mfma_f32_32x32x16_bf16 v[82:97], v[78:81], v[162:165], v[82:97]
	ds_read_b128 v[18:21], v233 offset:128
	ds_read_b128 v[22:25], v233 offset:144
	ds_read_b128 v[26:29], v233 offset:160
	ds_read_b128 v[30:33], v233 offset:176
	v_exp_f32_e32 v212, v36
	v_exp_f32_e32 v213, v40
	v_exp_f32_e32 v214, v44
	v_exp_f32_e32 v215, v48
	s_waitcnt lgkmcnt(4)
	s_barrier
	v_mfma_f32_32x32x16_bf16 v[82:97], v[74:77], v[166:169], v[82:97]
	ds_read_b128 v[130:133], v158 offset:0
	ds_read_b128 v[134:137], v159 offset:0
	v_exp_f32_e32 v216, v34
	v_fma_f32 v251, v212, s12, s12
	v_exp_f32_e32 v217, v38
	v_fma_f32 v252, v213, s12, s12
	v_exp_f32_e32 v218, v42
	v_fma_f32 v253, v214, s12, s12
	v_exp_f32_e32 v219, v46
	v_fma_f32 v254, v215, s12, s12
	v_mfma_f32_32x32x16_bf16 v[82:97], v[70:73], v[170:173], v[82:97]
	ds_read_b128 v[138:141], v160 offset:0
	ds_read_b128 v[142:145], v161 offset:0
	v_exp_f32_e32 v220, v35
	v_fmac_f32_e32 v251, v216, v251
	v_exp_f32_e32 v221, v39
	v_fmac_f32_e32 v252, v217, v252
	v_exp_f32_e32 v222, v43
	v_fmac_f32_e32 v253, v218, v253
	v_exp_f32_e32 v223, v47
	v_fmac_f32_e32 v254, v219, v254
	v_mfma_f32_32x32x16_bf16 v[82:97], v[66:69], v[174:177], v[82:97]
	ds_read_b128 v[146:149], v190 offset:0
	ds_read_b128 v[150:153], v191 offset:0
	v_rcp_f32_e32 v216, v251
	v_add_f32_e32 v220, 1.0, v220
	v_rcp_f32_e32 v217, v252
	v_add_f32_e32 v221, 1.0, v221
	v_rcp_f32_e32 v218, v253
	v_add_f32_e32 v222, 1.0, v222
	v_rcp_f32_e32 v219, v254
	v_add_f32_e32 v223, 1.0, v223
	v_mfma_f32_32x32x16_bf16 v[82:97], v[62:65], v[178:181], v[82:97]
	ds_read_b128 v[154:157], v192 offset:0
	v_rcp_f32_e32 v220, v220
	v_fma_f32 v240, -v212, v216, v216
	v_rcp_f32_e32 v221, v221
	v_fma_f32 v241, -v213, v217, v217
	v_rcp_f32_e32 v222, v222
	v_fma_f32 v242, -v214, v218, v218
	v_rcp_f32_e32 v223, v223
	v_fma_f32 v243, -v215, v219, v219
	v_mfma_f32_32x32x16_bf16 v[82:97], v[58:61], v[182:185], v[82:97]
	v_exp_f32_e32 v246, v37
	v_fma_f32 v202, v220, v202, v240
	v_exp_f32_e32 v247, v41
	v_fma_f32 v203, v221, v203, v241
	v_exp_f32_e32 v248, v45
	v_fma_f32 v204, v222, v204, v242
	v_exp_f32_e32 v249, v49
	v_fma_f32 v205, v223, v205, v243
	v_mfma_f32_32x32x16_bf16 v[82:97], v[54:57], v[186:189], v[82:97]
	v_exp_f32_e32 v212, v202
	v_add_f32_e32 v246, 1.0, v246
	v_exp_f32_e32 v213, v203
	v_add_f32_e32 v247, 1.0, v247
	v_exp_f32_e32 v214, v204
	v_add_f32_e32 v248, 1.0, v248
	v_exp_f32_e32 v215, v205
	v_add_f32_e32 v249, 1.0, v249
	v_fmac_f32_e32 v246, v246, v212
	v_fmac_f32_e32 v247, v247, v213
	v_fmac_f32_e32 v248, v248, v214
	v_fmac_f32_e32 v249, v249, v215
	v_mfma_f32_32x32x16_bf16 v[82:97], v[50:53], v[224:227], v[82:97]
	v_rcp_f32_e32 v246, v246
	v_rcp_f32_e32 v247, v247
	v_rcp_f32_e32 v248, v248
	v_rcp_f32_e32 v249, v249
	v_fma_f32 v246, -v212, v246, v246
	v_fma_f32 v247, -v213, v247, v247
	v_fma_f32 v248, -v214, v248, v248
	v_fma_f32 v249, -v215, v249, v249
	v_cvt_pk_bf16_f32 v224, v246, v247
	v_cvt_pk_bf16_f32 v225, v248, v249
	s_waitcnt lgkmcnt(0)
	v_mfma_f32_32x32x16_bf16 v[2:17], v[126:129], v[130:133], v[2:17]
	v_add_u32_e32 v234, v231, v245
	ds_read_b128 v[34:37], v234 offset:0
	ds_read_b128 v[38:41], v234 offset:16
	ds_read_b128 v[42:45], v234 offset:32
	ds_read_b128 v[46:49], v234 offset:48
	v_add_u32_e32 v232, 0x100, v232
	v_exp_f32_e32 v212, v84
	v_exp_f32_e32 v213, v88
	v_exp_f32_e32 v214, v92
	v_exp_f32_e32 v215, v96
	v_mfma_f32_32x32x16_bf16 v[2:17], v[122:125], v[134:137], v[2:17]
	v_exp_f32_e32 v216, v82
	v_fma_f32 v251, v212, s12, s12
	v_exp_f32_e32 v217, v86
	v_fma_f32 v252, v213, s12, s12
	v_exp_f32_e32 v218, v90
	v_fma_f32 v253, v214, s12, s12
	v_exp_f32_e32 v219, v94
	v_fma_f32 v254, v215, s12, s12
	v_mfma_f32_32x32x16_bf16 v[2:17], v[118:121], v[138:141], v[2:17]
	v_exp_f32_e32 v220, v83
	v_fmac_f32_e32 v251, v216, v251
	v_exp_f32_e32 v221, v87
	v_fmac_f32_e32 v252, v217, v252
	v_exp_f32_e32 v222, v91
	v_fmac_f32_e32 v253, v218, v253
	v_exp_f32_e32 v223, v95
	v_fmac_f32_e32 v254, v219, v254
	v_mfma_f32_32x32x16_bf16 v[2:17], v[114:117], v[142:145], v[2:17]
	v_rcp_f32_e32 v216, v251
	v_add_f32_e32 v220, 1.0, v220
	v_rcp_f32_e32 v217, v252
	v_add_f32_e32 v221, 1.0, v221
	v_rcp_f32_e32 v218, v253
	v_add_f32_e32 v222, 1.0, v222
	v_rcp_f32_e32 v219, v254
	v_add_f32_e32 v223, 1.0, v223
	v_mfma_f32_32x32x16_bf16 v[2:17], v[110:113], v[146:149], v[2:17]
	v_rcp_f32_e32 v220, v220
	v_fma_f32 v240, -v212, v216, v216
	v_rcp_f32_e32 v221, v221
	v_fma_f32 v241, -v213, v217, v217
	v_rcp_f32_e32 v222, v222
	v_fma_f32 v242, -v214, v218, v218
	v_rcp_f32_e32 v223, v223
	v_fma_f32 v243, -v215, v219, v219
	v_mfma_f32_32x32x16_bf16 v[2:17], v[106:109], v[150:153], v[2:17]
	v_exp_f32_e32 v246, v85
	v_fma_f32 v206, v220, v206, v240
	v_exp_f32_e32 v247, v89
	v_fma_f32 v207, v221, v207, v241
	v_exp_f32_e32 v248, v93
	v_fma_f32 v208, v222, v208, v242
	v_exp_f32_e32 v249, v97
	v_fma_f32 v209, v223, v209, v243
	v_mfma_f32_32x32x16_bf16 v[2:17], v[102:105], v[154:157], v[2:17]
	v_exp_f32_e32 v212, v206
	v_add_f32_e32 v246, 1.0, v246
	v_exp_f32_e32 v213, v207
	v_add_f32_e32 v247, 1.0, v247
	v_exp_f32_e32 v214, v208
	v_add_f32_e32 v248, 1.0, v248
	v_exp_f32_e32 v215, v209
	v_add_f32_e32 v249, 1.0, v249
	v_fmac_f32_e32 v246, v246, v212
	v_fmac_f32_e32 v247, v247, v213
	v_fmac_f32_e32 v248, v248, v214
	v_fmac_f32_e32 v249, v249, v215
	v_mfma_f32_32x32x16_bf16 v[2:17], v[98:101], v[236:239], v[2:17]
	v_rcp_f32_e32 v246, v246
	v_rcp_f32_e32 v247, v247
	v_rcp_f32_e32 v248, v248
	v_rcp_f32_e32 v249, v249
	v_fma_f32 v246, -v212, v246, v246
	v_fma_f32 v247, -v213, v247, v247
	v_fma_f32 v248, -v214, v248, v248
	v_fma_f32 v249, -v215, v249, v249
	v_cvt_pk_bf16_f32 v226, v246, v247
	v_cvt_pk_bf16_f32 v227, v248, v249
	ds_write_b128 v211, v[224:227] offset:8192
	s_sub_u32 s16, s16, 1
	s_cmp_lg_u32 s16, 0
	s_cbranch_scc1 .Llight_loop
	v_mfma_f32_32x32x16_bf16 v[18:33], v[78:81], v[130:133], v[18:33]
	ds_read_b128 v[82:85], v234 offset:128
	ds_read_b128 v[86:89], v234 offset:144
	ds_read_b128 v[90:93], v234 offset:160
	ds_read_b128 v[94:97], v234 offset:176
	v_exp_f32_e32 v212, v4
	v_exp_f32_e32 v213, v8
	v_exp_f32_e32 v214, v12
	v_exp_f32_e32 v215, v16
	s_waitcnt lgkmcnt(4)
	s_barrier
	v_mfma_f32_32x32x16_bf16 v[18:33], v[74:77], v[134:137], v[18:33]
	ds_read_b128 v[162:165], v158 offset:8192
	ds_read_b128 v[166:169], v159 offset:8192
	v_exp_f32_e32 v216, v2
	v_fma_f32 v251, v212, s12, s12
	v_exp_f32_e32 v217, v6
	v_fma_f32 v252, v213, s12, s12
	v_exp_f32_e32 v218, v10
	v_fma_f32 v253, v214, s12, s12
	v_exp_f32_e32 v219, v14
	v_fma_f32 v254, v215, s12, s12
	v_mfma_f32_32x32x16_bf16 v[18:33], v[70:73], v[138:141], v[18:33]
	ds_read_b128 v[170:173], v160 offset:8192
	ds_read_b128 v[174:177], v161 offset:8192
	v_exp_f32_e32 v220, v3
	v_fmac_f32_e32 v251, v216, v251
	v_exp_f32_e32 v221, v7
	v_fmac_f32_e32 v252, v217, v252
	v_exp_f32_e32 v222, v11
	v_fmac_f32_e32 v253, v218, v253
	v_exp_f32_e32 v223, v15
	v_fmac_f32_e32 v254, v219, v254
	v_mfma_f32_32x32x16_bf16 v[18:33], v[66:69], v[142:145], v[18:33]
	ds_read_b128 v[178:181], v190 offset:8192
	ds_read_b128 v[182:185], v191 offset:8192
	v_rcp_f32_e32 v216, v251
	v_add_f32_e32 v220, 1.0, v220
	v_rcp_f32_e32 v217, v252
	v_add_f32_e32 v221, 1.0, v221
	v_rcp_f32_e32 v218, v253
	v_add_f32_e32 v222, 1.0, v222
	v_rcp_f32_e32 v219, v254
	v_add_f32_e32 v223, 1.0, v223
	v_mfma_f32_32x32x16_bf16 v[18:33], v[62:65], v[146:149], v[18:33]
	ds_read_b128 v[186:189], v192 offset:8192
	v_rcp_f32_e32 v220, v220
	v_fma_f32 v240, -v212, v216, v216
	v_rcp_f32_e32 v221, v221
	v_fma_f32 v241, -v213, v217, v217
	v_rcp_f32_e32 v222, v222
	v_fma_f32 v242, -v214, v218, v218
	v_rcp_f32_e32 v223, v223
	v_fma_f32 v243, -v215, v219, v219
	v_mfma_f32_32x32x16_bf16 v[18:33], v[58:61], v[150:153], v[18:33]
	v_exp_f32_e32 v246, v5
	v_fma_f32 v194, v220, v194, v240
	v_exp_f32_e32 v247, v9
	v_fma_f32 v195, v221, v195, v241
	v_exp_f32_e32 v248, v13
	v_fma_f32 v196, v222, v196, v242
	v_exp_f32_e32 v249, v17
	v_fma_f32 v197, v223, v197, v243
	v_mfma_f32_32x32x16_bf16 v[18:33], v[54:57], v[154:157], v[18:33]
	v_exp_f32_e32 v212, v194
	v_add_f32_e32 v246, 1.0, v246
	v_exp_f32_e32 v213, v195
	v_add_f32_e32 v247, 1.0, v247
	v_exp_f32_e32 v214, v196
	v_add_f32_e32 v248, 1.0, v248
	v_exp_f32_e32 v215, v197
	v_add_f32_e32 v249, 1.0, v249
	v_fmac_f32_e32 v246, v246, v212
	v_fmac_f32_e32 v247, v247, v213
	v_fmac_f32_e32 v248, v248, v214
	v_fmac_f32_e32 v249, v249, v215
	v_mfma_f32_32x32x16_bf16 v[18:33], v[50:53], v[236:239], v[18:33]
	v_rcp_f32_e32 v246, v246
	v_rcp_f32_e32 v247, v247
	v_rcp_f32_e32 v248, v248
	v_rcp_f32_e32 v249, v249
	v_fma_f32 v246, -v212, v246, v246
	v_fma_f32 v247, -v213, v247, v247
	v_fma_f32 v248, -v214, v248, v248
	v_fma_f32 v249, -v215, v249, v249
	v_cvt_pk_bf16_f32 v236, v246, v247
	v_cvt_pk_bf16_f32 v237, v248, v249
	s_waitcnt lgkmcnt(0)
	v_mfma_f32_32x32x16_bf16 v[34:49], v[126:129], v[162:165], v[34:49]
	v_exp_f32_e32 v212, v20
	v_exp_f32_e32 v213, v24
	v_exp_f32_e32 v214, v28
	v_exp_f32_e32 v215, v32
	v_mfma_f32_32x32x16_bf16 v[34:49], v[122:125], v[166:169], v[34:49]
	v_exp_f32_e32 v216, v18
	v_fma_f32 v251, v212, s12, s12
	v_exp_f32_e32 v217, v22
	v_fma_f32 v252, v213, s12, s12
	v_exp_f32_e32 v218, v26
	v_fma_f32 v253, v214, s12, s12
	v_exp_f32_e32 v219, v30
	v_fma_f32 v254, v215, s12, s12
	v_mfma_f32_32x32x16_bf16 v[34:49], v[118:121], v[170:173], v[34:49]
	v_exp_f32_e32 v220, v19
	v_fmac_f32_e32 v251, v216, v251
	v_exp_f32_e32 v221, v23
	v_fmac_f32_e32 v252, v217, v252
	v_exp_f32_e32 v222, v27
	v_fmac_f32_e32 v253, v218, v253
	v_exp_f32_e32 v223, v31
	v_fmac_f32_e32 v254, v219, v254
	v_mfma_f32_32x32x16_bf16 v[34:49], v[114:117], v[174:177], v[34:49]
	v_rcp_f32_e32 v216, v251
	v_add_f32_e32 v220, 1.0, v220
	v_rcp_f32_e32 v217, v252
	v_add_f32_e32 v221, 1.0, v221
	v_rcp_f32_e32 v218, v253
	v_add_f32_e32 v222, 1.0, v222
	v_rcp_f32_e32 v219, v254
	v_add_f32_e32 v223, 1.0, v223
	v_mfma_f32_32x32x16_bf16 v[34:49], v[110:113], v[178:181], v[34:49]
	v_rcp_f32_e32 v220, v220
	v_fma_f32 v240, -v212, v216, v216
	v_rcp_f32_e32 v221, v221
	v_fma_f32 v241, -v213, v217, v217
	v_rcp_f32_e32 v222, v222
	v_fma_f32 v242, -v214, v218, v218
	v_rcp_f32_e32 v223, v223
	v_fma_f32 v243, -v215, v219, v219
	v_mfma_f32_32x32x16_bf16 v[34:49], v[106:109], v[182:185], v[34:49]
	v_exp_f32_e32 v246, v21
	v_fma_f32 v198, v220, v198, v240
	v_exp_f32_e32 v247, v25
	v_fma_f32 v199, v221, v199, v241
	v_exp_f32_e32 v248, v29
	v_fma_f32 v200, v222, v200, v242
	v_exp_f32_e32 v249, v33
	v_fma_f32 v201, v223, v201, v243
	v_mfma_f32_32x32x16_bf16 v[34:49], v[102:105], v[186:189], v[34:49]
	v_exp_f32_e32 v212, v198
	v_add_f32_e32 v246, 1.0, v246
	v_exp_f32_e32 v213, v199
	v_add_f32_e32 v247, 1.0, v247
	v_exp_f32_e32 v214, v200
	v_add_f32_e32 v248, 1.0, v248
	v_exp_f32_e32 v215, v201
	v_add_f32_e32 v249, 1.0, v249
	v_fmac_f32_e32 v246, v246, v212
	v_fmac_f32_e32 v247, v247, v213
	v_fmac_f32_e32 v248, v248, v214
	v_fmac_f32_e32 v249, v249, v215
	v_mfma_f32_32x32x16_bf16 v[34:49], v[98:101], v[224:227], v[34:49]
	v_rcp_f32_e32 v246, v246
	v_rcp_f32_e32 v247, v247
	v_rcp_f32_e32 v248, v248
	v_rcp_f32_e32 v249, v249
	v_fma_f32 v246, -v212, v246, v246
	v_fma_f32 v247, -v213, v247, v247
	v_fma_f32 v248, -v214, v248, v248
	v_fma_f32 v249, -v215, v249, v249
	v_cvt_pk_bf16_f32 v238, v246, v247
	v_cvt_pk_bf16_f32 v239, v248, v249
	ds_write_b128 v211, v[236:239] offset:0
	s_waitcnt lgkmcnt(0)
	s_barrier
	s_bfe_u32 s20, s19, 0x10006
	s_lshl_b32 s21, s20, 7
	s_lshl_b32 s20, s20, 13
	s_add_u32 s20, s20, 0x30000
	s_add_u32 s22, s14, s20
	s_addc_u32 s23, s15, 0
	s_add_u32 s24, s22, 0x1000
	s_addc_u32 s25, s23, 0
	global_load_dwordx4 v[98:101], v210, s[22:23] offset:0
	global_load_dwordx4 v[102:105], v210, s[22:23] offset:1024
	global_load_dwordx4 v[106:109], v210, s[22:23] offset:2048
	global_load_dwordx4 v[110:113], v210, s[22:23] offset:3072
	global_load_dwordx4 v[114:117], v210, s[24:25] offset:0
	global_load_dwordx4 v[118:121], v210, s[24:25] offset:1024
	global_load_dwordx4 v[122:125], v210, s[24:25] offset:2048
	global_load_dwordx4 v[126:129], v210, s[24:25] offset:3072
	v_or_b32_e32 v250, s21, v230
	global_load_dwordx4 v[130:133], v250, s[4:5] offset:0
	global_load_dwordx4 v[134:137], v250, s[4:5] offset:32
	global_load_dwordx4 v[138:141], v250, s[4:5] offset:64
	global_load_dwordx4 v[142:145], v250, s[4:5] offset:96
	global_load_dwordx4 v[146:149], v250, s[6:7] offset:0
	global_load_dwordx4 v[150:153], v250, s[6:7] offset:32
	global_load_dwordx4 v[154:157], v250, s[6:7] offset:64
	global_load_dwordx4 v[158:161], v250, s[6:7] offset:96
	s_load_dword s26, s[8:9], 0x0
	v_mfma_f32_32x32x16_bf16 v[82:97], v[78:81], v[162:165], v[82:97]
	v_exp_f32_e32 v212, v36
	v_exp_f32_e32 v213, v40
	v_exp_f32_e32 v214, v44
	v_exp_f32_e32 v215, v48
	v_mfma_f32_32x32x16_bf16 v[82:97], v[74:77], v[166:169], v[82:97]
	v_exp_f32_e32 v216, v34
	v_fma_f32 v251, v212, s12, s12
	v_exp_f32_e32 v217, v38
	v_fma_f32 v252, v213, s12, s12
	v_exp_f32_e32 v218, v42
	v_fma_f32 v253, v214, s12, s12
	v_exp_f32_e32 v219, v46
	v_fma_f32 v254, v215, s12, s12
	v_mfma_f32_32x32x16_bf16 v[82:97], v[70:73], v[170:173], v[82:97]
	v_exp_f32_e32 v220, v35
	v_fmac_f32_e32 v251, v216, v251
	v_exp_f32_e32 v221, v39
	v_fmac_f32_e32 v252, v217, v252
	v_exp_f32_e32 v222, v43
	v_fmac_f32_e32 v253, v218, v253
	v_exp_f32_e32 v223, v47
	v_fmac_f32_e32 v254, v219, v254
	v_mfma_f32_32x32x16_bf16 v[82:97], v[66:69], v[174:177], v[82:97]
	v_rcp_f32_e32 v216, v251
	v_add_f32_e32 v220, 1.0, v220
	v_rcp_f32_e32 v217, v252
	v_add_f32_e32 v221, 1.0, v221
	v_rcp_f32_e32 v218, v253
	v_add_f32_e32 v222, 1.0, v222
	v_rcp_f32_e32 v219, v254
	v_add_f32_e32 v223, 1.0, v223
	v_mfma_f32_32x32x16_bf16 v[82:97], v[62:65], v[178:181], v[82:97]
	v_rcp_f32_e32 v220, v220
	v_fma_f32 v240, -v212, v216, v216
	v_rcp_f32_e32 v221, v221
	v_fma_f32 v241, -v213, v217, v217
	v_rcp_f32_e32 v222, v222
	v_fma_f32 v242, -v214, v218, v218
	v_rcp_f32_e32 v223, v223
	v_fma_f32 v243, -v215, v219, v219
	v_mfma_f32_32x32x16_bf16 v[82:97], v[58:61], v[182:185], v[82:97]
	v_exp_f32_e32 v246, v37
	v_fma_f32 v202, v220, v202, v240
	v_exp_f32_e32 v247, v41
	v_fma_f32 v203, v221, v203, v241
	v_exp_f32_e32 v248, v45
	v_fma_f32 v204, v222, v204, v242
	v_exp_f32_e32 v249, v49
	v_fma_f32 v205, v223, v205, v243
	v_mfma_f32_32x32x16_bf16 v[82:97], v[54:57], v[186:189], v[82:97]
	v_exp_f32_e32 v212, v202
	v_add_f32_e32 v246, 1.0, v246
	v_exp_f32_e32 v213, v203
	v_add_f32_e32 v247, 1.0, v247
	v_exp_f32_e32 v214, v204
	v_add_f32_e32 v248, 1.0, v248
	v_exp_f32_e32 v215, v205
	v_add_f32_e32 v249, 1.0, v249
	v_fmac_f32_e32 v246, v246, v212
	v_fmac_f32_e32 v247, v247, v213
	v_fmac_f32_e32 v248, v248, v214
	v_fmac_f32_e32 v249, v249, v215
	v_mfma_f32_32x32x16_bf16 v[82:97], v[50:53], v[224:227], v[82:97]
	v_rcp_f32_e32 v246, v246
	v_rcp_f32_e32 v247, v247
	v_rcp_f32_e32 v248, v248
	v_rcp_f32_e32 v249, v249
	v_fma_f32 v246, -v212, v246, v246
	v_fma_f32 v247, -v213, v247, v247
	v_fma_f32 v248, -v214, v248, v248
	v_fma_f32 v249, -v215, v249, v249
	v_cvt_pk_bf16_f32 v224, v246, v247
	v_cvt_pk_bf16_f32 v225, v248, v249
	s_waitcnt lgkmcnt(0)
	v_exp_f32_e32 v212, v84
	v_exp_f32_e32 v213, v88
	v_exp_f32_e32 v214, v92
	v_exp_f32_e32 v215, v96
	v_exp_f32_e32 v216, v82
	v_fma_f32 v251, v212, s12, s12
	v_exp_f32_e32 v217, v86
	v_fma_f32 v252, v213, s12, s12
	v_exp_f32_e32 v218, v90
	v_fma_f32 v253, v214, s12, s12
	v_exp_f32_e32 v219, v94
	v_fma_f32 v254, v215, s12, s12
	v_exp_f32_e32 v220, v83
	v_fmac_f32_e32 v251, v216, v251
	v_exp_f32_e32 v221, v87
	v_fmac_f32_e32 v252, v217, v252
	v_exp_f32_e32 v222, v91
	v_fmac_f32_e32 v253, v218, v253
	v_exp_f32_e32 v223, v95
	v_fmac_f32_e32 v254, v219, v254
	v_rcp_f32_e32 v216, v251
	v_add_f32_e32 v220, 1.0, v220
	v_rcp_f32_e32 v217, v252
	v_add_f32_e32 v221, 1.0, v221
	v_rcp_f32_e32 v218, v253
	v_add_f32_e32 v222, 1.0, v222
	v_rcp_f32_e32 v219, v254
	v_add_f32_e32 v223, 1.0, v223
	v_rcp_f32_e32 v220, v220
	v_fma_f32 v240, -v212, v216, v216
	v_rcp_f32_e32 v221, v221
	v_fma_f32 v241, -v213, v217, v217
	v_rcp_f32_e32 v222, v222
	v_fma_f32 v242, -v214, v218, v218
	v_rcp_f32_e32 v223, v223
	v_fma_f32 v243, -v215, v219, v219
	v_exp_f32_e32 v246, v85
	v_fma_f32 v206, v220, v206, v240
	v_exp_f32_e32 v247, v89
	v_fma_f32 v207, v221, v207, v241
	v_exp_f32_e32 v248, v93
	v_fma_f32 v208, v222, v208, v242
	v_exp_f32_e32 v249, v97
	v_fma_f32 v209, v223, v209, v243
	v_exp_f32_e32 v212, v206
	v_add_f32_e32 v246, 1.0, v246
	v_exp_f32_e32 v213, v207
	v_add_f32_e32 v247, 1.0, v247
	v_exp_f32_e32 v214, v208
	v_add_f32_e32 v248, 1.0, v248
	v_exp_f32_e32 v215, v209
	v_add_f32_e32 v249, 1.0, v249
	v_fmac_f32_e32 v246, v246, v212
	v_fmac_f32_e32 v247, v247, v213
	v_fmac_f32_e32 v248, v248, v214
	v_fmac_f32_e32 v249, v249, v215
	v_rcp_f32_e32 v246, v246
	v_rcp_f32_e32 v247, v247
	v_rcp_f32_e32 v248, v248
	v_rcp_f32_e32 v249, v249
	v_fma_f32 v246, -v212, v246, v246
	v_fma_f32 v247, -v213, v247, v247
	v_fma_f32 v248, -v214, v248, v248
	v_fma_f32 v249, -v215, v249, v249
	v_cvt_pk_bf16_f32 v226, v246, v247
	v_cvt_pk_bf16_f32 v227, v248, v249
	ds_write_b128 v211, v[224:227] offset:8192
	s_waitcnt lgkmcnt(0)
	s_barrier
	s_lshl_b32 s20, s19, 6
	s_and_b32 s20, s20, 0x2000
	v_or_b32_e32 v20, s20, v210
	ds_read_b128 v[162:165], v20 offset:0
	ds_read_b128 v[166:169], v20 offset:1024
	ds_read_b128 v[170:173], v20 offset:2048
	ds_read_b128 v[174:177], v20 offset:3072
	ds_read_b128 v[178:181], v20 offset:4096
	ds_read_b128 v[182:185], v20 offset:5120
	ds_read_b128 v[186:189], v20 offset:6144
	ds_read_b128 v[190:193], v20 offset:7168
	s_bfe_u32 s20, s19, 0x10006
	s_lshl_b32 s20, s20, 9
	s_and_b32 s21, s19, 0x80
	s_or_b32 s20, s20, s21
	v_lshlrev_b32_e32 v19, 2, v229
	v_add3_u32 v19, s20, v19, v228
	s_waitcnt vmcnt(0)
	s_waitcnt lgkmcnt(7)
	v_mfma_f32_32x32x16_bf16 v[2:17], v[98:101], v[162:165], 0
	s_waitcnt lgkmcnt(6)
	v_mfma_f32_32x32x16_bf16 v[2:17], v[102:105], v[166:169], v[2:17]
	s_waitcnt lgkmcnt(5)
	v_mfma_f32_32x32x16_bf16 v[2:17], v[106:109], v[170:173], v[2:17]
	s_waitcnt lgkmcnt(4)
	v_mfma_f32_32x32x16_bf16 v[2:17], v[110:113], v[174:177], v[2:17]
	s_waitcnt lgkmcnt(3)
	v_mfma_f32_32x32x16_bf16 v[2:17], v[114:117], v[178:181], v[2:17]
	s_waitcnt lgkmcnt(2)
	v_mfma_f32_32x32x16_bf16 v[2:17], v[118:121], v[182:185], v[2:17]
	s_waitcnt lgkmcnt(1)
	v_mfma_f32_32x32x16_bf16 v[2:17], v[122:125], v[186:189], v[2:17]
	s_waitcnt lgkmcnt(0)
	v_mfma_f32_32x32x16_bf16 v[2:17], v[126:129], v[190:193], v[2:17]
	s_nop 15
	s_nop 3
	v_add_f32_e32 v2, v2, v130
	v_add_f32_e32 v3, v3, v131
	v_add_f32_e32 v4, v4, v132
	v_add_f32_e32 v5, v5, v133
	v_add_f32_e32 v6, v6, v134
	v_add_f32_e32 v7, v7, v135
	v_add_f32_e32 v8, v8, v136
	v_add_f32_e32 v9, v9, v137
	v_add_f32_e32 v10, v10, v138
	v_add_f32_e32 v11, v11, v139
	v_add_f32_e32 v12, v12, v140
	v_add_f32_e32 v13, v13, v141
	v_add_f32_e32 v14, v14, v142
	v_add_f32_e32 v15, v15, v143
	v_add_f32_e32 v16, v16, v144
	v_add_f32_e32 v17, v17, v145
	v_max_f32_e32 v2, 0, v2
	v_max_f32_e32 v3, 0, v3
	v_max_f32_e32 v4, 0, v4
	v_max_f32_e32 v5, 0, v5
	v_max_f32_e32 v6, 0, v6
	v_max_f32_e32 v7, 0, v7
	v_max_f32_e32 v8, 0, v8
	v_max_f32_e32 v9, 0, v9
	v_max_f32_e32 v10, 0, v10
	v_max_f32_e32 v11, 0, v11
	v_max_f32_e32 v12, 0, v12
	v_max_f32_e32 v13, 0, v13
	v_max_f32_e32 v14, 0, v14
	v_max_f32_e32 v15, 0, v15
	v_max_f32_e32 v16, 0, v16
	v_max_f32_e32 v17, 0, v17
	v_fma_f32 v18, v2, v146, 0
	v_fmac_f32_e32 v18, v3, v147
	v_fmac_f32_e32 v18, v4, v148
	v_fmac_f32_e32 v18, v5, v149
	v_fmac_f32_e32 v18, v6, v150
	v_fmac_f32_e32 v18, v7, v151
	v_fmac_f32_e32 v18, v8, v152
	v_fmac_f32_e32 v18, v9, v153
	v_fmac_f32_e32 v18, v10, v154
	v_fmac_f32_e32 v18, v11, v155
	v_fmac_f32_e32 v18, v12, v156
	v_fmac_f32_e32 v18, v13, v157
	v_fmac_f32_e32 v18, v14, v158
	v_fmac_f32_e32 v18, v15, v159
	v_fmac_f32_e32 v18, v16, v160
	v_fmac_f32_e32 v18, v17, v161
	ds_write_b32 v19, v18 offset:35904
	s_branch .LBB1_40
